# router top-8 threshold bisection: exact early exit when exactly 8 keys are >= the trial threshold (same selection), on top of the pipelined router loop
# speedup vs baseline: 1.0046x; 1.0006x over previous
.LBB0_2805:
	s_lshl_b32 s12, 1, s9
	s_or_b32 s12, s12, s8
	v_cmp_le_u32_e32 vcc, s12, v24
	s_bcnt1_i32_b64 s13, vcc
	v_cmp_le_u32_e32 vcc, s12, v23
	s_bcnt1_i32_b64 s14, vcc
	v_cmp_le_u32_e32 vcc, s12, v22
	s_add_i32 s13, s14, s13
	s_bcnt1_i32_b64 s14, vcc
	v_cmp_le_u32_e32 vcc, s12, v21
	s_add_i32 s13, s13, s14
	s_bcnt1_i32_b64 s14, vcc
	s_add_i32 s13, s13, s14
	s_cmp_gt_u32 s13, 7
	s_cselect_b32 s8, s12, s8
	s_cmp_eq_u32 s13, 8
	s_cbranch_scc1 .Lmy_bis_exit
	s_add_i32 s12, s9, -1
	s_lshl_b32 s12, 1, s12
	s_or_b32 s12, s12, s8
	v_cmp_le_u32_e32 vcc, s12, v24
	s_bcnt1_i32_b64 s13, vcc
	v_cmp_le_u32_e32 vcc, s12, v23
	s_bcnt1_i32_b64 s14, vcc
	v_cmp_le_u32_e32 vcc, s12, v22
	s_add_i32 s13, s14, s13
	s_bcnt1_i32_b64 s14, vcc
	v_cmp_le_u32_e32 vcc, s12, v21
	s_add_i32 s13, s13, s14
	s_bcnt1_i32_b64 s14, vcc
	s_add_i32 s13, s13, s14
	s_cmp_gt_u32 s13, 7
	s_cselect_b32 s8, s12, s8
	s_cmp_eq_u32 s13, 8
	s_cbranch_scc1 .Lmy_bis_exit
	s_add_i32 s12, s9, -2
	s_lshl_b32 s12, 1, s12
	s_or_b32 s12, s12, s8
	v_cmp_le_u32_e32 vcc, s12, v24
	s_bcnt1_i32_b64 s13, vcc
	v_cmp_le_u32_e32 vcc, s12, v23
	s_bcnt1_i32_b64 s14, vcc
	v_cmp_le_u32_e32 vcc, s12, v22
	s_add_i32 s13, s14, s13
	s_bcnt1_i32_b64 s14, vcc
	v_cmp_le_u32_e32 vcc, s12, v21
	s_add_i32 s13, s13, s14
	s_bcnt1_i32_b64 s14, vcc
	s_add_i32 s13, s13, s14
	s_cmp_gt_u32 s13, 7
	s_cselect_b32 s8, s12, s8
	s_cmp_eq_u32 s13, 8
	s_cbranch_scc1 .Lmy_bis_exit
	s_add_i32 s9, s9, -3
	s_lshl_b32 s12, 1, s9
	s_or_b32 s12, s12, s8
	v_cmp_le_u32_e32 vcc, s12, v24
	s_bcnt1_i32_b64 s13, vcc
	v_cmp_le_u32_e32 vcc, s12, v23
	s_bcnt1_i32_b64 s14, vcc
	v_cmp_le_u32_e32 vcc, s12, v22
	s_add_i32 s13, s14, s13
	s_bcnt1_i32_b64 s14, vcc
	v_cmp_le_u32_e32 vcc, s12, v21
	s_add_i32 s13, s13, s14
	s_bcnt1_i32_b64 s14, vcc
	s_add_i32 s13, s13, s14
	s_cmp_gt_u32 s13, 7
	s_cselect_b32 s8, s12, s8
	s_cmp_eq_u32 s13, 8
	s_cbranch_scc1 .Lmy_bis_exit
	v_sub_co_u32_e64 v25, s[12:13], s9, 1
	s_nop 0
	v_readfirstlane_b32 s9, v25
	s_and_b64 vcc, exec, s[12:13]
	s_cbranch_vccz .LBB0_2805
	s_branch .Lmy_bis_done
.Lmy_bis_exit:
	s_add_i32 s8, s12, -1
.Lmy_bis_done:
	v_cmp_lt_u32_e32 vcc, s8, v24
	v_cmp_lt_u32_e64 s[56:57], s8, v23
	s_bcnt1_i32_b64 s9, vcc
	v_cmp_eq_u32_e64 s[54:55], s8, v24
	s_bcnt1_i32_b64 s12, s[56:57]
	v_cmp_eq_u32_e64 s[58:59], s8, v23
	v_cmp_lt_u32_e64 s[60:61], s8, v22
	v_mbcnt_lo_u32_b32 v25, s54, 0
	s_add_i32 s9, s9, s12
	v_mbcnt_lo_u32_b32 v26, s58, 0
	v_cmp_eq_u32_e64 s[62:63], s8, v22
	s_bcnt1_i32_b64 s12, s[60:61]
	v_cmp_lt_u32_e64 s[64:65], s8, v21
	v_cmp_eq_u32_e64 s[66:67], s8, v21
	v_mbcnt_hi_u32_b32 v25, s55, v25
	v_mbcnt_hi_u32_b32 v26, s59, v26
	s_add_i32 s9, s9, s12
	v_mbcnt_lo_u32_b32 v22, s62, 0
	s_bcnt1_i32_b64 s8, s[64:65]
	v_mbcnt_lo_u32_b32 v21, s66, 0
	v_add_u32_e32 v25, v26, v25
	v_mbcnt_hi_u32_b32 v22, s63, v22
	s_add_i32 s9, s9, s8
	v_mbcnt_hi_u32_b32 v21, s67, v21
	v_add3_u32 v21, v22, v25, v21
	s_sub_i32 s14, 8, s9
	v_cmp_gt_i32_e64 s[68:69], s14, v21
	v_cndmask_b32_e64 v24, 0, 1, s[54:55]
	s_and_b64 s[8:9], s[54:55], s[68:69]
	v_addc_co_u32_e64 v22, s[54:55], 0, v21, s[54:55]
	v_cmp_gt_i32_e64 s[54:55], s14, v22
	v_cndmask_b32_e64 v23, 0, 1, s[58:59]
	s_and_b64 s[12:13], s[58:59], s[54:55]
	v_addc_co_u32_e64 v21, s[54:55], v21, v24, s[58:59]
	v_cmp_gt_i32_e64 s[54:55], s14, v21
	v_addc_co_u32_e64 v21, s[58:59], v22, v23, s[62:63]
	s_or_b64 s[58:59], vcc, s[8:9]
	s_nop 0
	v_cndmask_b32_e64 v23, 0, 1, s[58:59]
	v_cmp_ne_u32_e32 vcc, 0, v23
	s_or_b64 s[20:21], s[56:57], s[12:13]
	s_and_b64 s[22:23], s[62:63], s[54:55]
	v_cmp_gt_i32_e64 s[54:55], s14, v21
	v_mbcnt_lo_u32_b32 v21, vcc_lo, 0
	v_cndmask_b32_e64 v22, 0, 1, s[20:21]
	v_mbcnt_hi_u32_b32 v21, vcc_hi, v21
	v_cmp_ne_u32_e32 vcc, 0, v22
	s_or_b64 s[12:13], s[60:61], s[22:23]
	s_and_b64 s[54:55], s[66:67], s[54:55]
	v_mbcnt_lo_u32_b32 v24, vcc_lo, 0
	v_mbcnt_hi_u32_b32 v24, vcc_hi, v24
	v_add_u32_e32 v24, v24, v21
	v_cndmask_b32_e64 v21, 0, 1, s[12:13]
	v_cmp_ne_u32_e32 vcc, 0, v21
	s_or_b64 s[8:9], s[64:65], s[54:55]
	v_cndmask_b32_e64 v26, 0, 1, s[8:9]
	v_mbcnt_lo_u32_b32 v25, vcc_lo, 0
	v_mbcnt_hi_u32_b32 v25, vcc_hi, v25
	v_cmp_ne_u32_e32 vcc, 0, v26
	s_nop 1
	v_mbcnt_lo_u32_b32 v26, vcc_lo, 0
	v_mbcnt_hi_u32_b32 v26, vcc_hi, v26
	v_add3_u32 v24, v25, v24, v26
	s_and_saveexec_b64 s[22:23], s[58:59]
	s_cbranch_execz .LBB0_2808
	v_readlane_b32 s14, v254, 10
	s_nop 1
	v_lshl_add_u32 v25, v24, 2, s14
	v_add_u32_e32 v25, 0x400, v25
	ds_write2_b32 v25, v8, v12 offset1:8
